# E12: E10 + MoE tile->expert table staged once per phase in LDS; the per-unit global load + vmcnt(0) drain in the G1/G2 unit heads replaced by an LDS read
# speedup vs baseline: 1.0138x; 1.0138x over previous
.LBB0_1199:
	s_or_b64 exec, exec, s[0:1]
	v_readlane_b32 s0, v252, 2
	v_mov_b32_e32 v0, 0x108000
	v_readlane_b32 s1, v252, 3
	s_waitcnt lgkmcnt(0)
	s_barrier
	s_add_u32 s8, s0, 0x108000
	s_addc_u32 s9, s1, 0
	s_nop 0
	global_load_dword v0, v0, s[0:1]
	s_add_u32 s33, s0, 0x108100
	s_addc_u32 s50, s1, 0
	s_mov_b32 s100, s33
	s_mov_b32 s101, s50
	v_lshlrev_b32_e32 v240, 2, v226
	global_load_dword v241, v240, s[100:101]
	global_load_dword v242, v240, s[100:101] offset:2048
	v_add_u32_e32 v240, 0x21000, v240
	s_waitcnt vmcnt(0)
	ds_write_b32 v240, v241
	ds_write_b32 v240, v242 offset:2048
	s_waitcnt lgkmcnt(0)
	s_barrier
	v_readlane_b32 s0, v252, 0
	v_mov_b32_e32 v6, v226
	v_readlane_b32 s1, v252, 1
	s_waitcnt vmcnt(0)
	v_lshlrev_b32_e32 v162, 4, v0
	v_cmp_ge_i32_e32 vcc, s0, v162
	v_readfirstlane_b32 s31, v0
	v_readfirstlane_b32 s6, v6
	v_cmp_lt_i32_e64 s[0:1], s0, v162
	s_cbranch_vccnz .LBB0_1201
	v_readlane_b32 s2, v252, 0
	s_mov_b32 s4, s2
	s_ashr_i32 s2, s2, 31
	s_lshr_b32 s2, s2, 29
	v_readlane_b32 s3, v252, 1
	s_add_i32 s2, s4, s2
	s_and_b32 s3, s2, -8
	s_sub_i32 s3, s4, s3
	v_mov_b32_e32 v0, s3
	v_alignbit_b32 v0, s31, v0, 31
	s_ashr_i32 s2, s2, 3
	v_readfirstlane_b32 s4, v0
	s_mul_i32 s3, s4, s3
	s_add_i32 s2, s3, s2
	s_ashr_i32 s3, s2, 31
	s_lshr_b32 s3, s3, 25
	s_add_i32 s3, s2, s3
	s_ashr_i32 s4, s3, 7
	s_lshl_b32 s4, s4, 3
	s_sub_i32 s5, s31, s4
	s_min_i32 s5, s5, 8
	s_abs_i32 s7, s5
	v_cvt_f32_u32_e32 v0, s7
	s_sub_i32 s11, 0, s7
	s_and_b32 s3, s3, 0xffffff80
	s_sub_i32 s2, s2, s3
	v_rcp_iflag_f32_e32 v0, v0
	s_abs_i32 s3, s2
	s_xor_b32 s10, s2, s5
	s_ashr_i32 s10, s10, 31
	v_mul_f32_e32 v0, 0x4f7ffffe, v0
	v_cvt_u32_f32_e32 v0, v0
	s_nop 0
	v_readfirstlane_b32 s12, v0
	s_mul_i32 s11, s11, s12
	s_mul_hi_u32 s11, s12, s11
	s_add_i32 s12, s12, s11
	s_mul_hi_u32 s11, s3, s12
	s_mul_i32 s12, s11, s7
	s_sub_i32 s3, s3, s12
	s_add_i32 s13, s11, 1
	s_sub_i32 s12, s3, s7
	s_cmp_ge_u32 s3, s7
	s_cselect_b32 s11, s13, s11
	s_cselect_b32 s3, s12, s3
	s_add_i32 s12, s11, 1
	s_cmp_ge_u32 s3, s7
	s_cselect_b32 s3, s12, s11
	s_xor_b32 s3, s3, s10
	s_sub_i32 s10, s3, s10
	s_mul_i32 s3, s10, s5
	s_sub_i32 s2, s2, s3
	s_add_i32 s16, s4, s2
	s_ashr_i32 s17, s16, 31
	s_lshl_b64 s[2:3], s[16:17], 2
	s_add_u32 s2, s33, s2
	s_addc_u32 s3, s50, s3
	v_mov_b32_e32 v0, 0
	global_load_dword v0, v0, s[2:3]
	s_waitcnt vmcnt(0)
	v_readfirstlane_b32 s40, v0

.LBB0_1209:
	s_add_i32 s71, s41, 1
	v_readlane_b32 s6, v252, 6
	s_mul_i32 s0, s71, s51
	v_readlane_b32 s7, v252, 7
	s_mul_hi_u32 s1, s71, s6
	s_add_i32 s1, s1, s0
	s_mul_i32 s0, s71, s6
	v_readlane_b32 s6, v252, 0
	v_readlane_b32 s7, v252, 1
	s_add_u32 s6, s0, s6
	s_addc_u32 s7, s1, s52
	v_cmp_ge_i64_e32 vcc, s[6:7], v[162:163]
	v_cmp_lt_i64_e64 s[0:1], s[6:7], v[162:163]
	s_cbranch_vccnz .LBB0_1211
	s_ashr_i32 s7, s6, 31
	s_lshr_b32 s7, s7, 29
	s_add_i32 s7, s6, s7
	s_ashr_i32 s34, s7, 3
	s_and_b32 s7, s7, -8
	s_sub_i32 s6, s6, s7
	s_cmp_lt_i32 s6, 0
	s_cselect_b32 s7, s66, s65
	s_mul_i32 s6, s6, s7
	s_add_i32 s6, s6, s34
	s_ashr_i32 s7, s6, 31
	s_lshr_b32 s7, s7, 25
	s_add_i32 s7, s6, s7
	s_ashr_i32 s34, s7, 7
	s_lshl_b32 s35, s34, 3
	s_sub_i32 s34, s31, s35
	s_min_i32 s36, s34, 8
	s_abs_i32 s34, s36
	v_cvt_f32_u32_e32 v0, s34
	s_sub_i32 s38, 0, s34
	s_and_b32 s7, s7, 0xffffff80
	s_sub_i32 s6, s6, s7
	v_rcp_iflag_f32_e32 v0, v0
	s_abs_i32 s7, s6
	s_xor_b32 s37, s6, s36
	s_ashr_i32 s37, s37, 31
	v_mul_f32_e32 v0, 0x4f7ffffe, v0
	v_cvt_u32_f32_e32 v0, v0
	s_nop 0
	v_readfirstlane_b32 s39, v0
	s_mul_i32 s38, s38, s39
	s_mul_hi_u32 s38, s39, s38
	s_add_i32 s39, s39, s38
	s_mul_hi_u32 s38, s7, s39
	s_mul_i32 s39, s38, s34
	s_sub_i32 s7, s7, s39
	s_add_i32 s44, s38, 1
	s_sub_i32 s39, s7, s34
	s_cmp_ge_u32 s7, s34
	s_cselect_b32 s38, s44, s38
	s_cselect_b32 s7, s39, s7
	s_add_i32 s39, s38, 1
	s_cmp_ge_u32 s7, s34
	s_cselect_b32 s7, s39, s38
	s_xor_b32 s7, s7, s37
	s_sub_i32 s34, s7, s37
	s_mul_i32 s7, s34, s36
	s_sub_i32 s6, s6, s7
	s_add_i32 s36, s35, s6
	s_ashr_i32 s37, s36, 31
	s_lshl_b32 s6, s36, 2
	s_add_i32 s6, s6, 0x21000
	v_mov_b32_e32 v0, s6
	ds_read_b32 v0, v0
	s_waitcnt lgkmcnt(0)
	v_readfirstlane_b32 s38, v0

.LBB0_1213:
	s_add_u32 s35, s42, 0x100
	s_addc_u32 s37, s43, 0
	s_mov_b32 s39, -2
	s_mov_b64 s[42:43], 0
	ds_read_b128 v[70:73], v190
	ds_read_b128 v[74:77], v190 offset:1024
	ds_read_b128 v[78:81], v190 offset:2048
	ds_read_b128 v[82:85], v190 offset:3072
	ds_read_b128 v[94:97], v191
	ds_read_b128 v[98:101], v191 offset:1024
	ds_read_b128 v[102:105], v191 offset:2048
	ds_read_b128 v[106:109], v191 offset:3072
	s_add_u32 s44, s42, 0x100
	s_addc_u32 s45, s43, 0
	s_add_u32 s48, s35, s42
	s_addc_u32 s49, s37, s43
	s_cmp_eq_u32 s39, 12
	s_cselect_b64 vcc, -1, 0
	s_and_b64 s[46:47], vcc, exec
	s_cselect_b32 s73, 0, s44
	s_cselect_b32 s72, 0, s45
	s_cselect_b32 s46, s0, s48
	s_cselect_b32 s47, s1, s49
	s_add_u32 s48, s14, s73
	s_addc_u32 s49, s15, s72
	s_add_i32 m0, s11, 0xc000
	s_add_u32 s42, s24, s42
	s_addc_u32 s43, s25, s43
	ds_read_b128 v[176:179], v192
	ds_read_b128 v[180:183], v192 offset:1024
	ds_read_b128 v[194:197], v192 offset:2048
	ds_read_b128 v[198:201], v192 offset:3072
	ds_read_b128 v[202:205], v192 offset:4096
	ds_read_b128 v[206:209], v192 offset:5120
	ds_read_b128 v[210:213], v192 offset:6144
	ds_read_b128 v[214:217], v192 offset:7168
	global_load_lds_dwordx4 v187, s[42:43]
	s_add_i32 m0, s11, 0xe000
	v_mov_b32_e32 v0, v172
	global_load_lds_dwordx4 v186, s[42:43]
	v_mov_b32_e32 v169, v173
	v_lshlrev_b32_e32 v184, 11, v0
	v_lshlrev_b32_e32 v185, 11, v169
	v_bfe_u32 v0, v0, 16, 16
	v_bfe_u32 v169, v169, 16, 16
	v_and_b32_e32 v184, 0x7fff800, v184
	v_and_b32_e32 v185, 0x7fff800, v185
	v_lshl_add_u32 v0, v0, 11, v175
	v_lshl_add_u32 v169, v169, 11, v175
	v_add_u32_e32 v184, v184, v175
	v_add_u32_e32 v185, v185, v175
	v_cndmask_b32_e32 v168, v168, v0, vcc
	v_cndmask_b32_e32 v186, v186, v169, vcc
	v_cndmask_b32_e32 v170, v170, v184, vcc
	v_cndmask_b32_e32 v187, v187, v185, vcc
	s_waitcnt vmcnt(8)
	s_waitcnt lgkmcnt(0)
	s_barrier
	s_setprio 1
	s_waitcnt lgkmcnt(0)
	v_mfma_i32_16x16x64_i8 v[158:161], v[70:73], v[176:179], 0
	v_mfma_i32_16x16x64_i8 v[150:153], v[78:81], v[176:179], 0
	v_mfma_i32_16x16x64_i8 v[142:145], v[70:73], v[194:197], 0
	v_mfma_i32_16x16x64_i8 v[134:137], v[78:81], v[194:197], 0
	v_mfma_i32_16x16x64_i8 v[126:129], v[70:73], v[202:205], 0
	v_mfma_i32_16x16x64_i8 v[118:121], v[78:81], v[202:205], 0
	v_mfma_i32_16x16x64_i8 v[110:113], v[70:73], v[210:213], 0
	v_mfma_i32_16x16x64_i8 v[86:89], v[78:81], v[210:213], 0
	v_mfma_i32_16x16x64_i8 v[158:161], v[74:77], v[180:183], v[158:161]
	v_mfma_i32_16x16x64_i8 v[150:153], v[82:85], v[180:183], v[150:153]
	v_mfma_i32_16x16x64_i8 v[142:145], v[74:77], v[198:201], v[142:145]
	v_mfma_i32_16x16x64_i8 v[134:137], v[82:85], v[198:201], v[134:137]
	v_mfma_i32_16x16x64_i8 v[126:129], v[74:77], v[206:209], v[126:129]
	v_mfma_i32_16x16x64_i8 v[118:121], v[82:85], v[206:209], v[118:121]
	v_mfma_i32_16x16x64_i8 v[110:113], v[74:77], v[214:217], v[110:113]
	v_mfma_i32_16x16x64_i8 v[86:89], v[82:85], v[214:217], v[86:89]
	s_setprio 0
	s_setprio 1
	v_mfma_i32_16x16x64_i8 v[154:157], v[94:97], v[176:179], 0
	v_mfma_i32_16x16x64_i8 v[146:149], v[102:105], v[176:179], 0
	v_mfma_i32_16x16x64_i8 v[138:141], v[94:97], v[194:197], 0
	v_mfma_i32_16x16x64_i8 v[130:133], v[102:105], v[194:197], 0
	v_mfma_i32_16x16x64_i8 v[122:125], v[94:97], v[202:205], 0
	v_mfma_i32_16x16x64_i8 v[114:117], v[102:105], v[202:205], 0
	v_mfma_i32_16x16x64_i8 v[90:93], v[94:97], v[210:213], 0
	v_mfma_i32_16x16x64_i8 v[66:69], v[102:105], v[210:213], 0
	v_mfma_i32_16x16x64_i8 v[154:157], v[98:101], v[180:183], v[154:157]
	v_mfma_i32_16x16x64_i8 v[146:149], v[106:109], v[180:183], v[146:149]
	v_mfma_i32_16x16x64_i8 v[138:141], v[98:101], v[198:201], v[138:141]
	v_mfma_i32_16x16x64_i8 v[130:133], v[106:109], v[198:201], v[130:133]
	v_mfma_i32_16x16x64_i8 v[122:125], v[98:101], v[206:209], v[122:125]
	v_mfma_i32_16x16x64_i8 v[114:117], v[106:109], v[206:209], v[114:117]
	v_mfma_i32_16x16x64_i8 v[90:93], v[98:101], v[214:217], v[90:93]
	v_mfma_i32_16x16x64_i8 v[66:69], v[106:109], v[214:217], v[66:69]
	s_setprio 0
	s_barrier
	s_add_i32 s42, s67, s57
	v_lshl_add_u64 v[184:185], s[46:47], 0, v[164:165]
	s_mov_b32 m0, s42
	ds_read_b128 v[176:179], v192 offset:16384
	ds_read_b128 v[180:183], v192 offset:17408
	ds_read_b128 v[194:197], v192 offset:18432
	ds_read_b128 v[198:201], v192 offset:19456
	ds_read_b128 v[202:205], v192 offset:20480
	ds_read_b128 v[206:209], v192 offset:21504
	ds_read_b128 v[210:213], v192 offset:22528
	ds_read_b128 v[214:217], v192 offset:23552
	global_load_lds_dwordx4 v[184:185], off
	s_add_i32 m0, s42, 0x2000
	s_add_u32 s42, s46, 0x40000
	v_lshl_add_u64 v[218:219], s[46:47], 0, v[166:167]
	s_addc_u32 s43, s47, 0
	s_add_i32 s72, s68, s57
	global_load_lds_dwordx4 v[218:219], off
	v_lshl_add_u64 v[220:221], s[42:43], 0, v[164:165]
	s_mov_b32 m0, s72
	v_mov_b32_e32 v169, v171
	global_load_lds_dwordx4 v[220:221], off
	v_lshl_add_u64 v[220:221], s[42:43], 0, v[166:167]
	s_add_i32 m0, s72, 0x2000
	v_lshl_add_u64 v[222:223], s[48:49], 0, v[168:169]
	global_load_lds_dwordx4 v[220:221], off
	s_mov_b32 m0, s11
	v_lshl_add_u64 v[220:221], s[48:49], 0, v[170:171]
	global_load_lds_dwordx4 v170, s[48:49]
	s_mov_b32 m0, s58
	s_nop 0
	global_load_lds_dwordx4 v168, s[48:49]
	s_waitcnt vmcnt(8)
	s_waitcnt lgkmcnt(0)
	s_barrier
	s_setprio 1
	s_waitcnt lgkmcnt(0)
	v_mfma_i32_16x16x64_i8 v[62:65], v[70:73], v[176:179], 0
	v_mfma_i32_16x16x64_i8 v[54:57], v[78:81], v[176:179], 0
	v_mfma_i32_16x16x64_i8 v[46:49], v[70:73], v[194:197], 0
	v_mfma_i32_16x16x64_i8 v[38:41], v[78:81], v[194:197], 0
	v_mfma_i32_16x16x64_i8 v[30:33], v[70:73], v[202:205], 0
	v_mfma_i32_16x16x64_i8 v[22:25], v[78:81], v[202:205], 0
	v_mfma_i32_16x16x64_i8 v[14:17], v[70:73], v[210:213], 0
	v_mfma_i32_16x16x64_i8 v[6:9], v[78:81], v[210:213], 0
	v_mfma_i32_16x16x64_i8 v[62:65], v[74:77], v[180:183], v[62:65]
	v_mfma_i32_16x16x64_i8 v[54:57], v[82:85], v[180:183], v[54:57]
	v_mfma_i32_16x16x64_i8 v[46:49], v[74:77], v[198:201], v[46:49]
	v_mfma_i32_16x16x64_i8 v[38:41], v[82:85], v[198:201], v[38:41]
	v_mfma_i32_16x16x64_i8 v[30:33], v[74:77], v[206:209], v[30:33]
	v_mfma_i32_16x16x64_i8 v[22:25], v[82:85], v[206:209], v[22:25]
	v_mfma_i32_16x16x64_i8 v[14:17], v[74:77], v[214:217], v[14:17]
	v_mfma_i32_16x16x64_i8 v[6:9], v[82:85], v[214:217], v[6:9]
	s_setprio 0
	s_setprio 1
	v_mfma_i32_16x16x64_i8 v[58:61], v[94:97], v[176:179], 0
	v_mfma_i32_16x16x64_i8 v[50:53], v[102:105], v[176:179], 0
	v_mfma_i32_16x16x64_i8 v[42:45], v[94:97], v[194:197], 0
	v_mfma_i32_16x16x64_i8 v[34:37], v[102:105], v[194:197], 0
	v_mfma_i32_16x16x64_i8 v[26:29], v[94:97], v[202:205], 0
	v_mfma_i32_16x16x64_i8 v[18:21], v[102:105], v[202:205], 0
	v_mfma_i32_16x16x64_i8 v[10:13], v[94:97], v[210:213], 0
	v_mfma_i32_16x16x64_i8 v[2:5], v[102:105], v[210:213], 0
	v_mfma_i32_16x16x64_i8 v[58:61], v[98:101], v[180:183], v[58:61]
	v_mfma_i32_16x16x64_i8 v[50:53], v[106:109], v[180:183], v[50:53]
	v_mfma_i32_16x16x64_i8 v[42:45], v[98:101], v[198:201], v[42:45]
	v_mfma_i32_16x16x64_i8 v[34:37], v[106:109], v[198:201], v[34:37]
	v_mfma_i32_16x16x64_i8 v[26:29], v[98:101], v[206:209], v[26:29]
	v_mfma_i32_16x16x64_i8 v[18:21], v[106:109], v[206:209], v[18:21]
	v_mfma_i32_16x16x64_i8 v[10:13], v[98:101], v[214:217], v[10:13]
	v_mfma_i32_16x16x64_i8 v[2:5], v[106:109], v[214:217], v[2:5]
	s_setprio 0
	s_barrier
	s_add_i32 s42, 0, 0x18000
	v_add_u32_e32 v0, s42, v189
	s_add_i32 s72, 0, 0x1c000
	ds_read_b128 v[70:73], v0
	ds_read_b128 v[74:77], v0 offset:1024
	ds_read_b128 v[78:81], v0 offset:2048
	ds_read_b128 v[82:85], v0 offset:3072
	v_add_u32_e32 v0, s72, v189
	ds_read_b128 v[94:97], v0
	ds_read_b128 v[98:101], v0 offset:1024
	ds_read_b128 v[102:105], v0 offset:2048
	ds_read_b128 v[106:109], v0 offset:3072
	s_mov_b32 m0, s59
	ds_read_b128 v[176:179], v192 offset:32768
	ds_read_b128 v[180:183], v192 offset:33792
	ds_read_b128 v[194:197], v192 offset:34816
	ds_read_b128 v[198:201], v192 offset:35840
	ds_read_b128 v[202:205], v192 offset:36864
	ds_read_b128 v[206:209], v192 offset:37888
	ds_read_b128 v[210:213], v192 offset:38912
	ds_read_b128 v[214:217], v192 offset:39936
	global_load_lds_dwordx4 v187, s[48:49]
	s_mov_b32 m0, s60
	s_nop 0
	global_load_lds_dwordx4 v186, s[48:49]
	s_waitcnt vmcnt(8)
	s_waitcnt lgkmcnt(0)
	s_barrier
	s_setprio 1
	s_waitcnt lgkmcnt(0)
	v_mfma_i32_16x16x64_i8 v[158:161], v[70:73], v[176:179], v[158:161]
	v_mfma_i32_16x16x64_i8 v[150:153], v[78:81], v[176:179], v[150:153]
	v_mfma_i32_16x16x64_i8 v[142:145], v[70:73], v[194:197], v[142:145]
	v_mfma_i32_16x16x64_i8 v[134:137], v[78:81], v[194:197], v[134:137]
	v_mfma_i32_16x16x64_i8 v[126:129], v[70:73], v[202:205], v[126:129]
	v_mfma_i32_16x16x64_i8 v[118:121], v[78:81], v[202:205], v[118:121]
	v_mfma_i32_16x16x64_i8 v[110:113], v[70:73], v[210:213], v[110:113]
	v_mfma_i32_16x16x64_i8 v[86:89], v[78:81], v[210:213], v[86:89]
	v_mfma_i32_16x16x64_i8 v[158:161], v[74:77], v[180:183], v[158:161]
	v_mfma_i32_16x16x64_i8 v[150:153], v[82:85], v[180:183], v[150:153]
	v_mfma_i32_16x16x64_i8 v[142:145], v[74:77], v[198:201], v[142:145]
	v_mfma_i32_16x16x64_i8 v[134:137], v[82:85], v[198:201], v[134:137]
	v_mfma_i32_16x16x64_i8 v[126:129], v[74:77], v[206:209], v[126:129]
	v_mfma_i32_16x16x64_i8 v[118:121], v[82:85], v[206:209], v[118:121]
	v_mfma_i32_16x16x64_i8 v[110:113], v[74:77], v[214:217], v[110:113]
	v_mfma_i32_16x16x64_i8 v[86:89], v[82:85], v[214:217], v[86:89]
	s_setprio 0
	s_setprio 1
	v_mfma_i32_16x16x64_i8 v[154:157], v[94:97], v[176:179], v[154:157]
	v_mfma_i32_16x16x64_i8 v[146:149], v[102:105], v[176:179], v[146:149]
	v_mfma_i32_16x16x64_i8 v[138:141], v[94:97], v[194:197], v[138:141]
	v_mfma_i32_16x16x64_i8 v[130:133], v[102:105], v[194:197], v[130:133]
	v_mfma_i32_16x16x64_i8 v[122:125], v[94:97], v[202:205], v[122:125]
	v_mfma_i32_16x16x64_i8 v[114:117], v[102:105], v[202:205], v[114:117]
	v_mfma_i32_16x16x64_i8 v[90:93], v[94:97], v[210:213], v[90:93]
	v_mfma_i32_16x16x64_i8 v[66:69], v[102:105], v[210:213], v[66:69]
	v_mfma_i32_16x16x64_i8 v[154:157], v[98:101], v[180:183], v[154:157]
	v_mfma_i32_16x16x64_i8 v[146:149], v[106:109], v[180:183], v[146:149]
	v_mfma_i32_16x16x64_i8 v[138:141], v[98:101], v[198:201], v[138:141]
	v_mfma_i32_16x16x64_i8 v[130:133], v[106:109], v[198:201], v[130:133]
	v_mfma_i32_16x16x64_i8 v[122:125], v[98:101], v[206:209], v[122:125]
	v_mfma_i32_16x16x64_i8 v[114:117], v[106:109], v[206:209], v[114:117]
	v_mfma_i32_16x16x64_i8 v[90:93], v[98:101], v[214:217], v[90:93]
	v_mfma_i32_16x16x64_i8 v[66:69], v[106:109], v[214:217], v[66:69]
	s_setprio 0
	s_barrier
	s_add_i32 s42, s42, s57
	v_lshl_add_u64 v[184:185], v[184:185], 0, s[22:23]
	s_mov_b32 m0, s42
	ds_read_b128 v[176:179], v192 offset:49152
	ds_read_b128 v[180:183], v192 offset:50176
	ds_read_b128 v[194:197], v192 offset:51200
	ds_read_b128 v[198:201], v192 offset:52224
	ds_read_b128 v[202:205], v192 offset:53248
	ds_read_b128 v[206:209], v192 offset:54272
	ds_read_b128 v[210:213], v192 offset:55296
	ds_read_b128 v[214:217], v192 offset:56320
	global_load_lds_dwordx4 v[184:185], off
	s_add_i32 m0, s42, 0x2000
	s_add_u32 s42, s46, 0x40080
	v_lshl_add_u64 v[184:185], v[218:219], 0, s[22:23]
	s_addc_u32 s43, s47, 0
	s_add_i32 s46, s72, s57
	global_load_lds_dwordx4 v[184:185], off
	v_lshl_add_u64 v[184:185], s[42:43], 0, v[164:165]
	s_mov_b32 m0, s46
	s_nop 0
	global_load_lds_dwordx4 v[184:185], off
	v_lshl_add_u64 v[184:185], s[42:43], 0, v[166:167]
	s_add_i32 m0, s46, 0x2000
	s_nop 0
	global_load_lds_dwordx4 v[184:185], off
	v_lshl_add_u64 v[184:185], v[220:221], 0, s[22:23]
	s_mov_b32 m0, s63
	s_nop 0
	global_load_lds_dwordx4 v[184:185], off
	v_lshl_add_u64 v[184:185], v[222:223], 0, s[22:23]
	s_mov_b32 m0, s64
	s_nop 0
	global_load_lds_dwordx4 v[184:185], off
	s_waitcnt vmcnt(8)
	s_waitcnt lgkmcnt(0)
	s_barrier
	s_setprio 1
	s_waitcnt lgkmcnt(0)
	v_mfma_i32_16x16x64_i8 v[62:65], v[70:73], v[176:179], v[62:65]
	v_mfma_i32_16x16x64_i8 v[54:57], v[78:81], v[176:179], v[54:57]
	v_mfma_i32_16x16x64_i8 v[46:49], v[70:73], v[194:197], v[46:49]
	v_mfma_i32_16x16x64_i8 v[38:41], v[78:81], v[194:197], v[38:41]
	v_mfma_i32_16x16x64_i8 v[30:33], v[70:73], v[202:205], v[30:33]
	v_mfma_i32_16x16x64_i8 v[22:25], v[78:81], v[202:205], v[22:25]
	v_mfma_i32_16x16x64_i8 v[14:17], v[70:73], v[210:213], v[14:17]
	v_mfma_i32_16x16x64_i8 v[6:9], v[78:81], v[210:213], v[6:9]
	v_mfma_i32_16x16x64_i8 v[62:65], v[74:77], v[180:183], v[62:65]
	v_mfma_i32_16x16x64_i8 v[54:57], v[82:85], v[180:183], v[54:57]
	v_mfma_i32_16x16x64_i8 v[46:49], v[74:77], v[198:201], v[46:49]
	v_mfma_i32_16x16x64_i8 v[38:41], v[82:85], v[198:201], v[38:41]
	v_mfma_i32_16x16x64_i8 v[30:33], v[74:77], v[206:209], v[30:33]
	v_mfma_i32_16x16x64_i8 v[22:25], v[82:85], v[206:209], v[22:25]
	v_mfma_i32_16x16x64_i8 v[14:17], v[74:77], v[214:217], v[14:17]
	v_mfma_i32_16x16x64_i8 v[6:9], v[82:85], v[214:217], v[6:9]
	s_setprio 0
	s_setprio 1
	v_mfma_i32_16x16x64_i8 v[58:61], v[94:97], v[176:179], v[58:61]
	v_mfma_i32_16x16x64_i8 v[50:53], v[102:105], v[176:179], v[50:53]
	v_mfma_i32_16x16x64_i8 v[42:45], v[94:97], v[194:197], v[42:45]
	v_mfma_i32_16x16x64_i8 v[34:37], v[102:105], v[194:197], v[34:37]
	v_mfma_i32_16x16x64_i8 v[26:29], v[94:97], v[202:205], v[26:29]
	v_mfma_i32_16x16x64_i8 v[18:21], v[102:105], v[202:205], v[18:21]
	v_mfma_i32_16x16x64_i8 v[10:13], v[94:97], v[210:213], v[10:13]
	v_mfma_i32_16x16x64_i8 v[2:5], v[102:105], v[210:213], v[2:5]
	v_mfma_i32_16x16x64_i8 v[58:61], v[98:101], v[180:183], v[58:61]
	v_mfma_i32_16x16x64_i8 v[50:53], v[106:109], v[180:183], v[50:53]
	v_mfma_i32_16x16x64_i8 v[42:45], v[98:101], v[198:201], v[42:45]
	v_mfma_i32_16x16x64_i8 v[34:37], v[106:109], v[198:201], v[34:37]
	v_mfma_i32_16x16x64_i8 v[26:29], v[98:101], v[206:209], v[26:29]
	v_mfma_i32_16x16x64_i8 v[18:21], v[106:109], v[206:209], v[18:21]
	v_mfma_i32_16x16x64_i8 v[10:13], v[98:101], v[214:217], v[10:13]
	v_mfma_i32_16x16x64_i8 v[2:5], v[106:109], v[214:217], v[2:5]
	s_setprio 0
	s_barrier
	s_add_i32 s39, s39, 2
	s_cmp_gt_u32 s39, 13
	s_mov_b64 s[42:43], s[44:45]
	s_cbranch_scc0 .LBB0_1214
	s_branch .Lkexit_1214
	s_nop 0
	s_nop 0
	s_nop 0
	s_nop 0
	s_nop 0
	s_nop 0
	s_nop 0
	s_nop 0
	s_nop 0
	s_nop 0
	s_nop 0
	s_nop 0
	s_nop 0
	s_nop 0
	s_nop 0
	s_nop 0
	s_nop 0
	s_nop 0
	s_nop 0
	s_nop 0
	s_nop 0
	s_nop 0
	s_nop 0
	s_nop 0
	s_nop 0
	s_nop 0
	s_nop 0

.LBB0_1352:
	s_or_b64 exec, exec, s[0:1]
	s_waitcnt lgkmcnt(0)
	v_mov_b32_e32 v1, 0
	s_barrier
	global_load_dword v0, v1, s[8:9]
	s_mov_b32 s100, s33
	s_mov_b32 s101, s50
	v_lshlrev_b32_e32 v240, 2, v226
	global_load_dword v241, v240, s[100:101]
	global_load_dword v242, v240, s[100:101] offset:2048
	v_add_u32_e32 v240, 0x21000, v240
	s_waitcnt vmcnt(0)
	ds_write_b32 v240, v241
	ds_write_b32 v240, v242 offset:2048
	s_waitcnt lgkmcnt(0)
	s_barrier
	v_readlane_b32 s4, v252, 0
	v_mov_b32_e32 v10, v226
	v_readlane_b32 s5, v252, 1
	s_mov_b32 s6, s4
	s_waitcnt vmcnt(0)
	v_readfirstlane_b32 s44, v0
	s_lshl_b32 s0, s44, 3
	s_cmp_lt_i32 s4, s0
	s_cselect_b64 s[4:5], -1, 0
	s_cmp_ge_i32 s6, s0
	v_readfirstlane_b32 s1, v10
	s_cbranch_scc1 .LBB0_1354
	v_readlane_b32 s6, v252, 0
	s_mov_b32 s8, s6
	s_ashr_i32 s6, s6, 31
	s_lshr_b32 s6, s6, 29
	v_readlane_b32 s7, v252, 1
	s_add_i32 s6, s8, s6
	s_ashr_i32 s7, s6, 3
	s_and_b32 s6, s6, -8
	s_sub_i32 s6, s8, s6
	s_lshr_b32 s8, s6, 31
	s_add_i32 s8, s44, s8
	s_mul_i32 s6, s8, s6
	s_add_i32 s6, s6, s7
	s_ashr_i32 s7, s6, 31
	s_lshr_b32 s7, s7, 26
	s_add_i32 s7, s6, s7
	s_ashr_i32 s8, s7, 6
	s_lshl_b32 s8, s8, 3
	s_sub_i32 s9, s44, s8
	s_min_i32 s9, s9, 8
	s_abs_i32 s12, s9
	v_cvt_f32_u32_e32 v0, s12
	s_sub_i32 s14, 0, s12
	s_andn2_b32 s7, s7, 63
	s_sub_i32 s6, s6, s7
	v_rcp_iflag_f32_e32 v0, v0
	s_abs_i32 s7, s6
	s_xor_b32 s13, s6, s9
	s_ashr_i32 s13, s13, 31
	v_mul_f32_e32 v0, 0x4f7ffffe, v0
	v_cvt_u32_f32_e32 v0, v0
	s_nop 0
	v_readfirstlane_b32 s15, v0
	s_mul_i32 s14, s14, s15
	s_mul_hi_u32 s14, s15, s14
	s_add_i32 s15, s15, s14
	s_mul_hi_u32 s14, s7, s15
	s_mul_i32 s15, s14, s12
	s_sub_i32 s7, s7, s15
	s_add_i32 s16, s14, 1
	s_sub_i32 s15, s7, s12
	s_cmp_ge_u32 s7, s12
	s_cselect_b32 s14, s16, s14
	s_cselect_b32 s7, s15, s7
	s_add_i32 s15, s14, 1
	s_cmp_ge_u32 s7, s12
	s_cselect_b32 s7, s15, s14
	s_xor_b32 s7, s7, s13
	s_sub_i32 s14, s7, s13
	s_mul_i32 s7, s14, s9
	s_sub_i32 s6, s6, s7
	s_add_i32 s16, s8, s6
	s_ashr_i32 s17, s16, 31
	s_lshl_b64 s[6:7], s[16:17], 2
	s_add_u32 s6, s33, s6
	s_addc_u32 s7, s50, s7
	global_load_dword v0, v1, s[6:7]
	s_waitcnt vmcnt(0)
	v_readfirstlane_b32 s38, v0

.LBB0_1362:
	s_andn2_b64 vcc, exec, s[34:35]
	s_cbranch_vccnz .LBB0_1364
	s_ashr_i32 s7, s6, 31
	s_lshr_b32 s7, s7, 29
	s_add_i32 s7, s6, s7
	s_ashr_i32 s26, s7, 3
	s_and_b32 s7, s7, -8
	s_sub_i32 s6, s6, s7
	s_lshr_b32 s7, s6, 31
	s_add_i32 s7, s44, s7
	s_mul_i32 s6, s6, s7
	s_add_i32 s6, s6, s26
	s_ashr_i32 s7, s6, 31
	s_lshr_b32 s7, s7, 26
	s_add_i32 s7, s6, s7
	s_ashr_i32 s26, s7, 6
	s_lshl_b32 s27, s26, 3
	s_sub_i32 s26, s44, s27
	s_min_i32 s28, s26, 8
	s_abs_i32 s26, s28
	v_cvt_f32_u32_e32 v0, s26
	s_sub_i32 s30, 0, s26
	s_andn2_b32 s7, s7, 63
	s_sub_i32 s6, s6, s7
	v_rcp_iflag_f32_e32 v0, v0
	s_abs_i32 s7, s6
	s_xor_b32 s29, s6, s28
	s_ashr_i32 s29, s29, 31
	v_mul_f32_e32 v0, 0x4f7ffffe, v0
	v_cvt_u32_f32_e32 v0, v0
	s_nop 0
	v_readfirstlane_b32 s31, v0
	s_mul_i32 s30, s30, s31
	s_mul_hi_u32 s30, s31, s30
	s_add_i32 s31, s31, s30
	s_mul_hi_u32 s30, s7, s31
	s_mul_i32 s31, s30, s26
	s_sub_i32 s7, s7, s31
	s_add_i32 s34, s30, 1
	s_sub_i32 s31, s7, s26
	s_cmp_ge_u32 s7, s26
	s_cselect_b32 s30, s34, s30
	s_cselect_b32 s7, s31, s7
	s_add_i32 s31, s30, 1
	s_cmp_ge_u32 s7, s26
	s_cselect_b32 s7, s31, s30
	s_xor_b32 s7, s7, s29
	s_sub_i32 s26, s7, s29
	s_mul_i32 s7, s26, s28
	s_sub_i32 s6, s6, s7
	s_add_i32 s28, s27, s6
	s_ashr_i32 s29, s28, 31
	s_lshl_b32 s6, s28, 2
	s_add_i32 s6, s6, 0x21000
	v_mov_b32_e32 v0, s6
	ds_read_b32 v0, v0
	s_waitcnt lgkmcnt(0)
	v_readfirstlane_b32 s30, v0

.LBB0_1366:
	s_lshl_b64 s[36:37], s[28:29], 19
	s_add_u32 s36, s2, s36
	s_addc_u32 s37, s3, s37
	s_and_b64 s[0:1], exec, s[0:1]
	s_cselect_b32 s27, s37, s43
	s_cselect_b32 s29, s36, s42
	s_add_u32 s0, s42, 0x40080
	s_addc_u32 s1, s43, 0
	s_add_u32 s31, s40, 0x100
	s_addc_u32 s39, s41, 0
	s_mov_b32 s61, -2
	ds_read_b128 v[66:69], v229
	ds_read_b128 v[70:73], v229 offset:1024
	ds_read_b128 v[82:85], v229 offset:2048
	ds_read_b128 v[86:89], v229 offset:3072
	ds_read_b128 v[90:93], v230
	ds_read_b128 v[94:97], v230 offset:1024
	ds_read_b128 v[98:101], v230 offset:2048
	ds_read_b128 v[102:105], v230 offset:3072
	s_add_u32 s40, s0, 0xfffc0080
	s_addc_u32 s41, s1, -1
	s_cmp_eq_u32 s61, 12
	s_cselect_b32 s43, s27, s41
	s_cselect_b32 s42, s29, s40
	s_cselect_b32 s41, s35, s39
	s_cselect_b32 s40, s34, s31
	v_lshl_add_u64 v[208:209], s[0:1], 0, v[170:171]
	s_add_i32 m0, s15, 0xc000
	ds_read_b128 v[176:179], v231
	ds_read_b128 v[180:183], v231 offset:1024
	ds_read_b128 v[184:187], v231 offset:2048
	ds_read_b128 v[188:191], v231 offset:3072
	ds_read_b128 v[192:195], v231 offset:4096
	ds_read_b128 v[196:199], v231 offset:5120
	ds_read_b128 v[200:203], v231 offset:6144
	ds_read_b128 v[204:207], v231 offset:7168
	global_load_lds_dwordx4 v[208:209], off
	v_lshl_add_u64 v[208:209], s[0:1], 0, v[172:173]
	s_add_i32 m0, s15, 0xe000
	s_nop 0
	global_load_lds_dwordx4 v[208:209], off
	s_waitcnt vmcnt(8)
	s_waitcnt lgkmcnt(0)
	s_barrier
	s_setprio 1
	s_waitcnt lgkmcnt(0)
	v_mfma_i32_16x16x64_i8 v[158:161], v[66:69], v[176:179], 0
	v_mfma_i32_16x16x64_i8 v[154:157], v[82:85], v[176:179], 0
	v_mfma_i32_16x16x64_i8 v[142:145], v[66:69], v[184:187], 0
	v_mfma_i32_16x16x64_i8 v[138:141], v[82:85], v[184:187], 0
	v_mfma_i32_16x16x64_i8 v[126:129], v[66:69], v[192:195], 0
	v_mfma_i32_16x16x64_i8 v[122:125], v[82:85], v[192:195], 0
	v_mfma_i32_16x16x64_i8 v[110:113], v[66:69], v[200:203], 0
	v_mfma_i32_16x16x64_i8 v[106:109], v[82:85], v[200:203], 0
	v_mfma_i32_16x16x64_i8 v[158:161], v[70:73], v[180:183], v[158:161]
	v_mfma_i32_16x16x64_i8 v[154:157], v[86:89], v[180:183], v[154:157]
	v_mfma_i32_16x16x64_i8 v[142:145], v[70:73], v[188:191], v[142:145]
	v_mfma_i32_16x16x64_i8 v[138:141], v[86:89], v[188:191], v[138:141]
	v_mfma_i32_16x16x64_i8 v[126:129], v[70:73], v[196:199], v[126:129]
	v_mfma_i32_16x16x64_i8 v[122:125], v[86:89], v[196:199], v[122:125]
	v_mfma_i32_16x16x64_i8 v[110:113], v[70:73], v[204:207], v[110:113]
	v_mfma_i32_16x16x64_i8 v[106:109], v[86:89], v[204:207], v[106:109]
	s_setprio 0
	s_setprio 1
	v_mfma_i32_16x16x64_i8 v[150:153], v[90:93], v[176:179], 0
	v_mfma_i32_16x16x64_i8 v[146:149], v[98:101], v[176:179], 0
	v_mfma_i32_16x16x64_i8 v[134:137], v[90:93], v[184:187], 0
	v_mfma_i32_16x16x64_i8 v[130:133], v[98:101], v[184:187], 0
	v_mfma_i32_16x16x64_i8 v[118:121], v[90:93], v[192:195], 0
	v_mfma_i32_16x16x64_i8 v[114:117], v[98:101], v[192:195], 0
	v_mfma_i32_16x16x64_i8 v[78:81], v[90:93], v[200:203], 0
	v_mfma_i32_16x16x64_i8 v[74:77], v[98:101], v[200:203], 0
	v_mfma_i32_16x16x64_i8 v[150:153], v[94:97], v[180:183], v[150:153]
	v_mfma_i32_16x16x64_i8 v[146:149], v[102:105], v[180:183], v[146:149]
	v_mfma_i32_16x16x64_i8 v[134:137], v[94:97], v[188:191], v[134:137]
	v_mfma_i32_16x16x64_i8 v[130:133], v[102:105], v[188:191], v[130:133]
	v_mfma_i32_16x16x64_i8 v[118:121], v[94:97], v[196:199], v[118:121]
	v_mfma_i32_16x16x64_i8 v[114:117], v[102:105], v[196:199], v[114:117]
	v_mfma_i32_16x16x64_i8 v[78:81], v[94:97], v[204:207], v[78:81]
	v_mfma_i32_16x16x64_i8 v[74:77], v[102:105], v[204:207], v[74:77]
	s_setprio 0
	s_barrier
	s_add_i32 s62, s57, s47
	v_lshl_add_u64 v[208:209], s[40:41], 0, v[164:165]
	s_mov_b32 m0, s62
	ds_read_b128 v[176:179], v231 offset:16384
	ds_read_b128 v[180:183], v231 offset:17408
	ds_read_b128 v[184:187], v231 offset:18432
	ds_read_b128 v[188:191], v231 offset:19456
	ds_read_b128 v[192:195], v231 offset:20480
	ds_read_b128 v[196:199], v231 offset:21504
	ds_read_b128 v[200:203], v231 offset:22528
	ds_read_b128 v[204:207], v231 offset:23552
	global_load_lds_dwordx4 v[208:209], off
	s_add_i32 m0, s62, 0x2000
	s_add_u32 s62, s40, 0x40000
	v_lshl_add_u64 v[210:211], s[40:41], 0, v[168:169]
	s_addc_u32 s63, s41, 0
	s_add_i32 s64, s58, s47
	global_load_lds_dwordx4 v[210:211], off
	v_lshl_add_u64 v[212:213], s[62:63], 0, v[164:165]
	s_mov_b32 m0, s64
	v_lshl_add_u64 v[214:215], s[42:43], 0, v[166:167]
	global_load_lds_dwordx4 v[212:213], off
	v_lshl_add_u64 v[212:213], s[62:63], 0, v[168:169]
	s_add_i32 m0, s64, 0x2000
	s_nop 0
	global_load_lds_dwordx4 v[212:213], off
	v_lshl_add_u64 v[212:213], s[42:43], 0, v[162:163]
	s_mov_b32 m0, s15
	s_nop 0
	global_load_lds_dwordx4 v[212:213], off
	s_mov_b32 m0, s48
	s_nop 0
	global_load_lds_dwordx4 v[214:215], off
	s_waitcnt vmcnt(8)
	s_waitcnt lgkmcnt(0)
	s_barrier
	s_setprio 1
	s_waitcnt lgkmcnt(0)
	v_mfma_i32_16x16x64_i8 v[62:65], v[66:69], v[176:179], 0
	v_mfma_i32_16x16x64_i8 v[58:61], v[82:85], v[176:179], 0
	v_mfma_i32_16x16x64_i8 v[46:49], v[66:69], v[184:187], 0
	v_mfma_i32_16x16x64_i8 v[42:45], v[82:85], v[184:187], 0
	v_mfma_i32_16x16x64_i8 v[30:33], v[66:69], v[192:195], 0
	v_mfma_i32_16x16x64_i8 v[26:29], v[82:85], v[192:195], 0
	v_mfma_i32_16x16x64_i8 v[14:17], v[66:69], v[200:203], 0
	v_mfma_i32_16x16x64_i8 v[10:13], v[82:85], v[200:203], 0
	v_mfma_i32_16x16x64_i8 v[62:65], v[70:73], v[180:183], v[62:65]
	v_mfma_i32_16x16x64_i8 v[58:61], v[86:89], v[180:183], v[58:61]
	v_mfma_i32_16x16x64_i8 v[46:49], v[70:73], v[188:191], v[46:49]
	v_mfma_i32_16x16x64_i8 v[42:45], v[86:89], v[188:191], v[42:45]
	v_mfma_i32_16x16x64_i8 v[30:33], v[70:73], v[196:199], v[30:33]
	v_mfma_i32_16x16x64_i8 v[26:29], v[86:89], v[196:199], v[26:29]
	v_mfma_i32_16x16x64_i8 v[14:17], v[70:73], v[204:207], v[14:17]
	v_mfma_i32_16x16x64_i8 v[10:13], v[86:89], v[204:207], v[10:13]
	s_setprio 0
	s_setprio 1
	v_mfma_i32_16x16x64_i8 v[54:57], v[90:93], v[176:179], 0
	v_mfma_i32_16x16x64_i8 v[50:53], v[98:101], v[176:179], 0
	v_mfma_i32_16x16x64_i8 v[38:41], v[90:93], v[184:187], 0
	v_mfma_i32_16x16x64_i8 v[34:37], v[98:101], v[184:187], 0
	v_mfma_i32_16x16x64_i8 v[22:25], v[90:93], v[192:195], 0
	v_mfma_i32_16x16x64_i8 v[18:21], v[98:101], v[192:195], 0
	v_mfma_i32_16x16x64_i8 v[6:9], v[90:93], v[200:203], 0
	v_mfma_i32_16x16x64_i8 v[2:5], v[98:101], v[200:203], 0
	v_mfma_i32_16x16x64_i8 v[54:57], v[94:97], v[180:183], v[54:57]
	v_mfma_i32_16x16x64_i8 v[50:53], v[102:105], v[180:183], v[50:53]
	v_mfma_i32_16x16x64_i8 v[38:41], v[94:97], v[188:191], v[38:41]
	v_mfma_i32_16x16x64_i8 v[34:37], v[102:105], v[188:191], v[34:37]
	v_mfma_i32_16x16x64_i8 v[22:25], v[94:97], v[196:199], v[22:25]
	v_mfma_i32_16x16x64_i8 v[18:21], v[102:105], v[196:199], v[18:21]
	v_mfma_i32_16x16x64_i8 v[6:9], v[94:97], v[204:207], v[6:9]
	v_mfma_i32_16x16x64_i8 v[2:5], v[102:105], v[204:207], v[2:5]
	s_setprio 0
	s_barrier
	s_add_i32 s62, 0, 0x18000
	v_add_u32_e32 v0, s62, v227
	s_add_i32 s63, 0, 0x1c000
	ds_read_b128 v[66:69], v0
	ds_read_b128 v[70:73], v0 offset:1024
	ds_read_b128 v[82:85], v0 offset:2048
	ds_read_b128 v[86:89], v0 offset:3072
	v_add_u32_e32 v0, s63, v227
	ds_read_b128 v[90:93], v0
	ds_read_b128 v[94:97], v0 offset:1024
	ds_read_b128 v[98:101], v0 offset:2048
	ds_read_b128 v[102:105], v0 offset:3072
	s_add_u32 s42, s42, 0x40000
	s_addc_u32 s43, s43, 0
	s_mov_b32 m0, s49
	v_lshl_add_u64 v[216:217], s[42:43], 0, v[162:163]
	ds_read_b128 v[176:179], v231 offset:32768
	ds_read_b128 v[180:183], v231 offset:33792
	ds_read_b128 v[184:187], v231 offset:34816
	ds_read_b128 v[188:191], v231 offset:35840
	ds_read_b128 v[192:195], v231 offset:36864
	ds_read_b128 v[196:199], v231 offset:37888
	ds_read_b128 v[200:203], v231 offset:38912
	ds_read_b128 v[204:207], v231 offset:39936
	global_load_lds_dwordx4 v[216:217], off
	v_lshl_add_u64 v[216:217], s[42:43], 0, v[166:167]
	s_mov_b32 m0, s51
	s_nop 0
	global_load_lds_dwordx4 v[216:217], off
	s_waitcnt vmcnt(8)
	s_waitcnt lgkmcnt(0)
	s_barrier
	s_setprio 1
	s_waitcnt lgkmcnt(0)
	v_mfma_i32_16x16x64_i8 v[158:161], v[66:69], v[176:179], v[158:161]
	v_mfma_i32_16x16x64_i8 v[154:157], v[82:85], v[176:179], v[154:157]
	v_mfma_i32_16x16x64_i8 v[142:145], v[66:69], v[184:187], v[142:145]
	v_mfma_i32_16x16x64_i8 v[138:141], v[82:85], v[184:187], v[138:141]
	v_mfma_i32_16x16x64_i8 v[126:129], v[66:69], v[192:195], v[126:129]
	v_mfma_i32_16x16x64_i8 v[122:125], v[82:85], v[192:195], v[122:125]
	v_mfma_i32_16x16x64_i8 v[110:113], v[66:69], v[200:203], v[110:113]
	v_mfma_i32_16x16x64_i8 v[106:109], v[82:85], v[200:203], v[106:109]
	v_mfma_i32_16x16x64_i8 v[158:161], v[70:73], v[180:183], v[158:161]
	v_mfma_i32_16x16x64_i8 v[154:157], v[86:89], v[180:183], v[154:157]
	v_mfma_i32_16x16x64_i8 v[142:145], v[70:73], v[188:191], v[142:145]
	v_mfma_i32_16x16x64_i8 v[138:141], v[86:89], v[188:191], v[138:141]
	v_mfma_i32_16x16x64_i8 v[126:129], v[70:73], v[196:199], v[126:129]
	v_mfma_i32_16x16x64_i8 v[122:125], v[86:89], v[196:199], v[122:125]
	v_mfma_i32_16x16x64_i8 v[110:113], v[70:73], v[204:207], v[110:113]
	v_mfma_i32_16x16x64_i8 v[106:109], v[86:89], v[204:207], v[106:109]
	s_setprio 0
	s_setprio 1
	v_mfma_i32_16x16x64_i8 v[150:153], v[90:93], v[176:179], v[150:153]
	v_mfma_i32_16x16x64_i8 v[146:149], v[98:101], v[176:179], v[146:149]
	v_mfma_i32_16x16x64_i8 v[134:137], v[90:93], v[184:187], v[134:137]
	v_mfma_i32_16x16x64_i8 v[130:133], v[98:101], v[184:187], v[130:133]
	v_mfma_i32_16x16x64_i8 v[118:121], v[90:93], v[192:195], v[118:121]
	v_mfma_i32_16x16x64_i8 v[114:117], v[98:101], v[192:195], v[114:117]
	v_mfma_i32_16x16x64_i8 v[78:81], v[90:93], v[200:203], v[78:81]
	v_mfma_i32_16x16x64_i8 v[74:77], v[98:101], v[200:203], v[74:77]
	v_mfma_i32_16x16x64_i8 v[150:153], v[94:97], v[180:183], v[150:153]
	v_mfma_i32_16x16x64_i8 v[146:149], v[102:105], v[180:183], v[146:149]
	v_mfma_i32_16x16x64_i8 v[134:137], v[94:97], v[188:191], v[134:137]
	v_mfma_i32_16x16x64_i8 v[130:133], v[102:105], v[188:191], v[130:133]
	v_mfma_i32_16x16x64_i8 v[118:121], v[94:97], v[196:199], v[118:121]
	v_mfma_i32_16x16x64_i8 v[114:117], v[102:105], v[196:199], v[114:117]
	v_mfma_i32_16x16x64_i8 v[78:81], v[94:97], v[204:207], v[78:81]
	v_mfma_i32_16x16x64_i8 v[74:77], v[102:105], v[204:207], v[74:77]
	s_setprio 0
	s_barrier
	s_add_i32 s42, s62, s47
	v_lshl_add_u64 v[208:209], v[208:209], 0, s[22:23]
	s_mov_b32 m0, s42
	ds_read_b128 v[176:179], v231 offset:49152
	ds_read_b128 v[180:183], v231 offset:50176
	ds_read_b128 v[184:187], v231 offset:51200
	ds_read_b128 v[188:191], v231 offset:52224
	ds_read_b128 v[192:195], v231 offset:53248
	ds_read_b128 v[196:199], v231 offset:54272
	ds_read_b128 v[200:203], v231 offset:55296
	ds_read_b128 v[204:207], v231 offset:56320
	global_load_lds_dwordx4 v[208:209], off
	s_add_i32 m0, s42, 0x2000
	s_add_u32 s40, s40, 0x40080
	v_lshl_add_u64 v[208:209], v[210:211], 0, s[22:23]
	s_addc_u32 s41, s41, 0
	s_add_i32 s42, s63, s47
	global_load_lds_dwordx4 v[208:209], off
	v_lshl_add_u64 v[208:209], s[40:41], 0, v[164:165]
	s_mov_b32 m0, s42
	s_nop 0
	global_load_lds_dwordx4 v[208:209], off
	v_lshl_add_u64 v[208:209], s[40:41], 0, v[168:169]
	s_add_i32 m0, s42, 0x2000
	s_nop 0
	global_load_lds_dwordx4 v[208:209], off
	v_lshl_add_u64 v[208:209], v[212:213], 0, s[22:23]
	s_mov_b32 m0, s53
	s_nop 0
	global_load_lds_dwordx4 v[208:209], off
	v_lshl_add_u64 v[208:209], v[214:215], 0, s[22:23]
	s_mov_b32 m0, s54
	s_nop 0
	global_load_lds_dwordx4 v[208:209], off
	s_waitcnt vmcnt(8)
	s_waitcnt lgkmcnt(0)
	s_barrier
	s_setprio 1
	s_waitcnt lgkmcnt(0)
	v_mfma_i32_16x16x64_i8 v[62:65], v[66:69], v[176:179], v[62:65]
	v_mfma_i32_16x16x64_i8 v[58:61], v[82:85], v[176:179], v[58:61]
	v_mfma_i32_16x16x64_i8 v[46:49], v[66:69], v[184:187], v[46:49]
	v_mfma_i32_16x16x64_i8 v[42:45], v[82:85], v[184:187], v[42:45]
	v_mfma_i32_16x16x64_i8 v[30:33], v[66:69], v[192:195], v[30:33]
	v_mfma_i32_16x16x64_i8 v[26:29], v[82:85], v[192:195], v[26:29]
	v_mfma_i32_16x16x64_i8 v[14:17], v[66:69], v[200:203], v[14:17]
	v_mfma_i32_16x16x64_i8 v[10:13], v[82:85], v[200:203], v[10:13]
	v_mfma_i32_16x16x64_i8 v[62:65], v[70:73], v[180:183], v[62:65]
	v_mfma_i32_16x16x64_i8 v[58:61], v[86:89], v[180:183], v[58:61]
	v_mfma_i32_16x16x64_i8 v[46:49], v[70:73], v[188:191], v[46:49]
	v_mfma_i32_16x16x64_i8 v[42:45], v[86:89], v[188:191], v[42:45]
	v_mfma_i32_16x16x64_i8 v[30:33], v[70:73], v[196:199], v[30:33]
	v_mfma_i32_16x16x64_i8 v[26:29], v[86:89], v[196:199], v[26:29]
	v_mfma_i32_16x16x64_i8 v[14:17], v[70:73], v[204:207], v[14:17]
	v_mfma_i32_16x16x64_i8 v[10:13], v[86:89], v[204:207], v[10:13]
	s_setprio 0
	s_setprio 1
	v_mfma_i32_16x16x64_i8 v[54:57], v[90:93], v[176:179], v[54:57]
	v_mfma_i32_16x16x64_i8 v[50:53], v[98:101], v[176:179], v[50:53]
	v_mfma_i32_16x16x64_i8 v[38:41], v[90:93], v[184:187], v[38:41]
	v_mfma_i32_16x16x64_i8 v[34:37], v[98:101], v[184:187], v[34:37]
	v_mfma_i32_16x16x64_i8 v[22:25], v[90:93], v[192:195], v[22:25]
	v_mfma_i32_16x16x64_i8 v[18:21], v[98:101], v[192:195], v[18:21]
	v_mfma_i32_16x16x64_i8 v[6:9], v[90:93], v[200:203], v[6:9]
	v_mfma_i32_16x16x64_i8 v[2:5], v[98:101], v[200:203], v[2:5]
	v_mfma_i32_16x16x64_i8 v[54:57], v[94:97], v[180:183], v[54:57]
	v_mfma_i32_16x16x64_i8 v[50:53], v[102:105], v[180:183], v[50:53]
	v_mfma_i32_16x16x64_i8 v[38:41], v[94:97], v[188:191], v[38:41]
	v_mfma_i32_16x16x64_i8 v[34:37], v[102:105], v[188:191], v[34:37]
	v_mfma_i32_16x16x64_i8 v[22:25], v[94:97], v[196:199], v[22:25]
	v_mfma_i32_16x16x64_i8 v[18:21], v[102:105], v[196:199], v[18:21]
	v_mfma_i32_16x16x64_i8 v[6:9], v[94:97], v[204:207], v[6:9]
	v_mfma_i32_16x16x64_i8 v[2:5], v[102:105], v[204:207], v[2:5]
	s_setprio 0
	s_barrier
	s_add_i32 s61, s61, 2
	s_add_u32 s0, s0, 0x100
	s_addc_u32 s1, s1, 0
	s_add_u32 s31, s31, 0x100
	s_addc_u32 s39, s39, 0
	s_cmp_gt_u32 s61, 13
	s_cbranch_scc0 .LBB0_1367
	s_branch .Lkexit_1367
	s_nop 0
	s_nop 0
	s_nop 0
	s_nop 0
	s_nop 0
	s_nop 0
	s_nop 0
	s_nop 0
	s_nop 0
	s_nop 0
	s_nop 0
	s_nop 0
	s_nop 0
	s_nop 0
	s_nop 0
	s_nop 0
	s_nop 0
	s_nop 0
	s_nop 0
	s_nop 0
	s_nop 0
	s_nop 0
	s_nop 0
